# MLA tile loop: counted lgkmcnt waits in front of the Q.K MFMAs (each MFMA waits only for its own two K fragment reads)
# speedup vs baseline: 1.0125x; 1.0060x over previous
.LBB0_714:
	s_mul_i32 s0, s3, 0x3000
	s_add_i32 s89, s0, 0
	s_cmp_gt_i32 s85, s74
	s_mov_b64 s[0:1], -1
	s_cbranch_scc1 .LBB0_716
	v_add_u32_e32 v2, s89, v190
	v_add_u32_e32 v1, s89, v188
	ds_read_b128 v[8:11], v2
	ds_read_b128 v[4:7], v1
	ds_read_b128 v[116:119], v1 offset:64
	ds_read_b128 v[124:127], v1 offset:128
	ds_read_b128 v[120:123], v2 offset:64
	ds_read_b128 v[128:131], v2 offset:128
	s_waitcnt lgkmcnt(4)
	v_mfma_f32_32x32x64_f8f6f4 v[100:115], v[4:11], v[132:139], 0
	ds_read_b128 v[4:7], v1 offset:6144
	ds_read_b128 v[156:159], v1 offset:6208
	ds_read_b128 v[8:11], v2 offset:6144
	ds_read_b128 v[164:167], v1 offset:6272
	ds_read_b128 v[160:163], v2 offset:6208
	ds_read_b128 v[168:171], v2 offset:6272
	s_waitcnt lgkmcnt(7)
	v_mfma_f32_32x32x64_f8f6f4 v[100:115], v[116:123], v[140:147], v[100:115]
	s_nop 0
	s_waitcnt lgkmcnt(6)
	v_mfma_f32_32x32x64_f8f6f4 v[100:115], v[124:131], v[148:155], v[100:115]
	s_waitcnt lgkmcnt(3)
	v_mfma_f32_32x32x64_f8f6f4 v[116:131], v[4:11], v[132:139], 0
	s_mov_b64 s[0:1], 0
	s_waitcnt lgkmcnt(1)
	v_mfma_f32_32x32x64_f8f6f4 v[116:131], v[156:163], v[140:147], v[116:131]
	s_waitcnt lgkmcnt(0)
	v_mfma_f32_32x32x64_f8f6f4 v[116:131], v[164:171], v[148:155], v[116:131]
